# adds norm2 pass-1 load batching (16 loads per iteration issued together)
# speedup vs baseline: 1.0245x; 1.0008x over previous
.LBB0_882:
	v_lshl_add_u64 v[4:5], v[0:1], 0, s[24:25]
	v_add_co_u32_e32 v2, vcc, 0x34000000, v4
	s_add_u32 s24, s24, 0x200
	s_nop 0
	v_addc_co_u32_e32 v3, vcc, 0, v5, vcc
	v_add_co_u32_e32 v4, vcc, 0x34008000, v4
	s_nop 0
	s_nop 0
	v_addc_co_u32_e32 v5, vcc, 0, v5, vcc
	s_addc_u32 s25, s25, 0
	global_load_dwordx4 v[186:189], v[2:3], off
	global_load_dwordx4 v[190:193], v[4:5], off
	global_load_dwordx4 v[194:197], v[2:3], off offset:64
	global_load_dwordx4 v[198:201], v[4:5], off offset:64
	global_load_dwordx4 v[202:205], v[2:3], off offset:128
	global_load_dwordx4 v[206:209], v[4:5], off offset:128
	global_load_dwordx4 v[210:213], v[2:3], off offset:192
	global_load_dwordx4 v[214:217], v[4:5], off offset:192
	global_load_dwordx4 v[228:231], v[2:3], off offset:256
	global_load_dwordx4 v[232:235], v[4:5], off offset:256
	global_load_dwordx4 v[236:239], v[2:3], off offset:320
	global_load_dwordx4 v[244:247], v[4:5], off offset:320
	global_load_dwordx4 v[248:251], v[2:3], off offset:384
	global_load_dwordx4 v[160:163], v[4:5], off offset:384
	global_load_dwordx4 v[164:167], v[2:3], off offset:448
	global_load_dwordx4 v[168:171], v[4:5], off offset:448
	s_cmpk_eq_i32 s24, 0x800
	s_waitcnt vmcnt(14)
	v_dot2c_f32_bf16_e32 v7, v186, v186
	v_dot2c_f32_bf16_e32 v7, v187, v187
	v_dot2c_f32_bf16_e32 v7, v188, v188
	v_dot2c_f32_bf16_e32 v7, v189, v189
	v_dot2c_f32_bf16_e32 v6, v190, v190
	v_dot2c_f32_bf16_e32 v6, v191, v191
	v_dot2c_f32_bf16_e32 v6, v192, v192
	v_dot2c_f32_bf16_e32 v6, v193, v193
	s_waitcnt vmcnt(12)
	v_dot2c_f32_bf16_e32 v7, v194, v194
	v_dot2c_f32_bf16_e32 v7, v195, v195
	v_dot2c_f32_bf16_e32 v7, v196, v196
	v_dot2c_f32_bf16_e32 v7, v197, v197
	v_dot2c_f32_bf16_e32 v6, v198, v198
	v_dot2c_f32_bf16_e32 v6, v199, v199
	v_dot2c_f32_bf16_e32 v6, v200, v200
	v_dot2c_f32_bf16_e32 v6, v201, v201
	s_waitcnt vmcnt(10)
	v_dot2c_f32_bf16_e32 v7, v202, v202
	v_dot2c_f32_bf16_e32 v7, v203, v203
	v_dot2c_f32_bf16_e32 v7, v204, v204
	v_dot2c_f32_bf16_e32 v7, v205, v205
	v_dot2c_f32_bf16_e32 v6, v206, v206
	v_dot2c_f32_bf16_e32 v6, v207, v207
	v_dot2c_f32_bf16_e32 v6, v208, v208
	v_dot2c_f32_bf16_e32 v6, v209, v209
	s_waitcnt vmcnt(8)
	v_dot2c_f32_bf16_e32 v7, v210, v210
	v_dot2c_f32_bf16_e32 v7, v211, v211
	v_dot2c_f32_bf16_e32 v7, v212, v212
	v_dot2c_f32_bf16_e32 v7, v213, v213
	v_dot2c_f32_bf16_e32 v6, v214, v214
	v_dot2c_f32_bf16_e32 v6, v215, v215
	v_dot2c_f32_bf16_e32 v6, v216, v216
	v_dot2c_f32_bf16_e32 v6, v217, v217
	s_waitcnt vmcnt(6)
	v_dot2c_f32_bf16_e32 v7, v228, v228
	v_dot2c_f32_bf16_e32 v7, v229, v229
	v_dot2c_f32_bf16_e32 v7, v230, v230
	v_dot2c_f32_bf16_e32 v7, v231, v231
	v_dot2c_f32_bf16_e32 v6, v232, v232
	v_dot2c_f32_bf16_e32 v6, v233, v233
	v_dot2c_f32_bf16_e32 v6, v234, v234
	v_dot2c_f32_bf16_e32 v6, v235, v235
	s_waitcnt vmcnt(4)
	v_dot2c_f32_bf16_e32 v7, v236, v236
	v_dot2c_f32_bf16_e32 v7, v237, v237
	v_dot2c_f32_bf16_e32 v7, v238, v238
	v_dot2c_f32_bf16_e32 v7, v239, v239
	v_dot2c_f32_bf16_e32 v6, v244, v244
	v_dot2c_f32_bf16_e32 v6, v245, v245
	v_dot2c_f32_bf16_e32 v6, v246, v246
	v_dot2c_f32_bf16_e32 v6, v247, v247
	s_waitcnt vmcnt(2)
	v_dot2c_f32_bf16_e32 v7, v248, v248
	v_dot2c_f32_bf16_e32 v7, v249, v249
	v_dot2c_f32_bf16_e32 v7, v250, v250
	v_dot2c_f32_bf16_e32 v7, v251, v251
	v_dot2c_f32_bf16_e32 v6, v160, v160
	v_dot2c_f32_bf16_e32 v6, v161, v161
	v_dot2c_f32_bf16_e32 v6, v162, v162
	v_dot2c_f32_bf16_e32 v6, v163, v163
	s_waitcnt vmcnt(0)
	v_dot2c_f32_bf16_e32 v7, v164, v164
	v_dot2c_f32_bf16_e32 v7, v165, v165
	v_dot2c_f32_bf16_e32 v7, v166, v166
	v_dot2c_f32_bf16_e32 v7, v167, v167
	v_dot2c_f32_bf16_e32 v6, v168, v168
	v_dot2c_f32_bf16_e32 v6, v169, v169
	v_dot2c_f32_bf16_e32 v6, v170, v170
	v_dot2c_f32_bf16_e32 v6, v171, v171
	s_cbranch_scc0 .LBB0_882
	s_lshl_b32 s50, s0, 8
	s_add_i32 s50, s50, s38
	v_or_b32_e32 v0, s50, v136
	v_ashrrev_i32_e32 v1, 31, v0
	v_lshlrev_b64 v[0:1], 11, v[0:1]
	v_lshl_add_u64 v[120:121], v[94:95], 0, v[0:1]
	v_mov_b32_e32 v0, v7
	s_nop 1
	v_permlane16_swap_b32 v7, v0
	v_mov_b32_e32 v36, v185
	v_add_f32_e32 v25, v7, v0
	v_mov_b32_e32 v29, v25
	v_mov_b32_e32 v0, v6
	s_nop 1
	v_permlane32_swap_b32 v25, v29
	s_nop 1
	v_permlane16_swap_b32 v6, v0
	v_mov_b32_e32 v28, v185
	v_add_f32_e32 v30, v6, v0
	v_add_co_u32_e32 v0, vcc, 0x8000, v120
	v_mov_b32_e32 v31, v30
	v_mov_b32_e32 v32, v185
	v_mov_b32_e32 v24, v185
	v_mov_b32_e32 v113, 0x43e00000
	v_addc_co_u32_e32 v1, vcc, 0, v121, vcc
	s_nop 1
	v_permlane32_swap_b32 v31, v30
	global_load_dwordx4 v[20:23], v[120:121], off
	global_load_dwordx4 v[16:19], v[0:1], off
	s_nop 0
	global_load_dwordx4 v[0:3], v[102:103], off
	global_load_dwordx4 v[4:7], v[104:105], off
	global_load_dwordx4 v[8:11], v[106:107], off
	global_load_dwordx4 v[12:15], v[108:109], off
	v_add_f32_e32 v25, v25, v29
	v_add_f32_e32 v29, v31, v30
	v_fmamk_f32 v25, v25, 0x3a800000, v252
	v_fmamk_f32 v29, v29, 0x3a800000, v252
	v_rsq_f32_e32 v126, v29
	v_rsq_f32_e32 v128, v25
	v_ashrrev_i32_e32 v115, 31, v114
	s_mov_b64 s[24:25], 0x8000
	v_lshlrev_b64 v[124:125], 10, v[114:115]
	v_lshl_add_u64 v[122:123], v[120:121], 0, s[24:25]
	v_or_b32_e32 v124, v96, v124
	v_lshl_add_u64 v[130:131], v[90:91], 0, v[26:27]
	v_mov_b32_e32 v127, v126
	v_mov_b32_e32 v129, v128
	s_mov_b32 s24, 64
	v_mov_b64_e32 v[132:133], v[116:117]
	v_mov_b32_e32 v115, v144
	v_mov_b32_e32 v37, v36
	v_mov_b32_e32 v38, v36
	v_mov_b32_e32 v39, v36
	v_mov_b32_e32 v29, v28
	v_mov_b32_e32 v30, v28
	v_mov_b32_e32 v31, v28
	v_mov_b32_e32 v33, v32
	v_mov_b32_e32 v34, v32
	v_mov_b32_e32 v35, v32
	v_mov_b32_e32 v25, v24
	v_mov_b32_e32 v26, v24
	v_mov_b32_e32 v27, v24
